# norm1 store phase: per row the (norm1_w, scale, shift) loads of column groups 1..3 hoisted to the group-0 loads with counted waits (three row blocks), on top of v82
# baseline (speedup 1.0000x reference)
.LBB0_172:
	global_load_dwordx4 v[58:61], v[74:75], off offset:-3072
	s_waitcnt lgkmcnt(2)
	global_load_dwordx4 v[50:53], v[74:75], off offset:-2048
	global_load_dwordx4 v[18:21], v[74:75], off
	s_waitcnt lgkmcnt(0)
	global_load_dwordx4 v[34:37], v[74:75], off offset:-1024
	s_add_i32 s19, s2, s6
	s_cmp_lt_i32 s19, 0x10000
	s_cselect_b32 s0, s19, s6
	s_ashr_i32 s1, s0, 31
	s_add_i32 s22, s3, s6
	s_lshl_b64 s[34:35], s[0:1], 12
	s_cmp_lt_i32 s22, 0x10000
	s_cselect_b64 s[24:25], -1, 0
	s_and_b64 s[0:1], s[24:25], exec
	s_cselect_b32 s0, s22, s6
	s_ashr_i32 s1, s0, 31
	s_add_i32 s18, s33, s6
	s_lshl_b64 s[30:31], s[0:1], 12
	s_cmp_lt_i32 s18, 0x10000
	s_cselect_b64 s[20:21], -1, 0
	s_and_b64 s[0:1], s[20:21], exec
	s_cselect_b32 s0, s18, s6
	s_ashr_i32 s23, s6, 13
	s_mul_i32 s26, s23, 0x1800
	s_ashr_i32 s1, s0, 31
	s_ashr_i32 s27, s26, 31
	s_lshl_b64 s[0:1], s[0:1], 12
	s_lshl_b64 s[26:27], s[26:27], 2
	s_add_u32 s26, s96, s26
	s_addc_u32 s27, s97, s27
	s_add_u32 s28, s26, 0x1000
	s_addc_u32 s29, s27, 0
	global_load_dwordx4 v[90:93], v86, s[28:29]
	global_load_dwordx4 v[94:97], v[66:67], off
	global_load_dwordx4 v[98:101], v86, s[26:27]
	s_cmp_gt_i32 s19, 0xffff
	s_waitcnt vmcnt(6)
	v_pk_mul_f32 v[2:3], v[60:61], v[60:61]
	v_pk_mul_f32 v[4:5], v[58:59], v[58:59]
	s_waitcnt vmcnt(5)
	v_pk_mul_f32 v[6:7], v[52:53], v[52:53]
	v_pk_mul_f32 v[8:9], v[50:51], v[50:51]
	v_pk_mov_b32 v[14:15], v[4:5], v[2:3] op_sel:[1,0]
	v_mov_b32_e32 v5, v3
	v_pk_mov_b32 v[2:3], v[8:9], v[6:7] op_sel:[1,0]
	v_mov_b32_e32 v9, v7
	s_waitcnt vmcnt(4)
	v_mul_f32_e32 v13, v18, v18
	s_waitcnt vmcnt(3)
	v_mul_f32_e32 v10, v35, v35
	v_mul_f32_e32 v12, v37, v37
	v_pk_add_f32 v[4:5], v[14:15], v[4:5]
	v_pk_add_f32 v[2:3], v[2:3], v[8:9]
	v_mul_f32_e32 v16, v19, v19
	v_mul_f32_e32 v17, v20, v20
	v_mul_f32_e32 v22, v21, v21
	v_pk_fma_f32 v[6:7], v[34:35], v[34:35], v[10:11] op_sel_hi:[1,1,0]
	v_pk_fma_f32 v[10:11], v[36:37], v[36:37], v[12:13] op_sel_hi:[1,1,0]
	v_pk_add_f32 v[4:5], v[4:5], v[4:5] op_sel:[0,1] op_sel_hi:[1,0]
	v_pk_add_f32 v[2:3], v[2:3], v[2:3] op_sel:[0,1] op_sel_hi:[1,0]
	v_mov_b32_e32 v7, v17
	v_mov_b32_e32 v11, v22
	v_mov_b32_e32 v5, v13
	v_mov_b32_e32 v3, v16
	v_pk_add_f32 v[6:7], v[6:7], v[10:11]
	v_pk_add_f32 v[2:3], v[4:5], v[2:3]
	s_waitcnt vmcnt(2)
	v_pk_add_f32 v[92:93], v[92:93], 1.0 op_sel_hi:[1,0]
	v_pk_add_f32 v[2:3], v[2:3], v[6:7]
	v_pk_add_f32 v[90:91], v[90:91], 1.0 op_sel_hi:[1,0]
	v_add_f32_e32 v2, v2, v3
	ds_bpermute_b32 v3, v1, v2
	s_waitcnt lgkmcnt(0)
	v_add_f32_e32 v2, v2, v3
	ds_bpermute_b32 v3, v79, v2
	s_waitcnt lgkmcnt(0)
	v_add_f32_e32 v4, v2, v3
	ds_bpermute_b32 v5, v80, v4
	v_lshl_add_u64 v[2:3], s[14:15], 0, v[70:71]
	v_add_co_u32_e32 v76, vcc, s9, v2
	s_waitcnt lgkmcnt(0)
	v_add_f32_e32 v4, v4, v5
	ds_bpermute_b32 v5, v81, v4
	v_addc_co_u32_e32 v77, vcc, 0, v3, vcc
	v_lshl_add_u64 v[2:3], v[68:69], 0, s[34:35]
	global_load_dwordx4 v[62:65], v[2:3], off
	global_load_dwordx4 v[54:57], v[2:3], off offset:1024
	s_waitcnt lgkmcnt(0)
	v_add_f32_e32 v4, v4, v5
	ds_bpermute_b32 v5, v82, v4
	global_load_dwordx4 v[46:49], v[2:3], off offset:2048
	global_load_dwordx4 v[42:45], v[2:3], off offset:3072
	v_lshl_add_u64 v[2:3], v[68:69], 0, s[30:31]
	global_load_dwordx4 v[38:41], v[2:3], off
	global_load_dwordx4 v[30:33], v[2:3], off offset:1024
	global_load_dwordx4 v[26:29], v[2:3], off offset:2048
	global_load_dwordx4 v[22:25], v[2:3], off offset:3072
	s_waitcnt lgkmcnt(0)
	v_add_f32_e32 v4, v4, v5
	ds_bpermute_b32 v5, v83, v4
	v_lshl_add_u64 v[2:3], v[68:69], 0, s[0:1]
	global_load_dwordx4 v[14:17], v[2:3], off
	global_load_dwordx4 v[10:13], v[2:3], off offset:1024
	s_waitcnt lgkmcnt(0)
	v_add_f32_e32 v4, v4, v5
	v_fmamk_f32 v4, v4, 0x3a800000, v84
	v_mul_f32_e32 v5, 0x4f800000, v4
	v_cmp_gt_f32_e32 vcc, s7, v4
	s_nop 1
	v_cndmask_b32_e32 v78, v4, v5, vcc
	v_sqrt_f32_e32 v102, v78
	global_load_dwordx4 v[6:9], v[2:3], off offset:2048
	s_nop 0
	global_load_dwordx4 v[2:5], v[2:3], off offset:3072
	v_add_u32_e32 v103, -1, v102
	v_add_u32_e32 v104, 1, v102
	v_fma_f32 v105, -v103, v102, v78
	v_fma_f32 v106, -v104, v102, v78
	v_cmp_ge_f32_e64 s[0:1], 0, v105
	s_nop 1
	v_cndmask_b32_e64 v102, v102, v103, s[0:1]
	v_cmp_lt_f32_e64 s[0:1], 0, v106
	s_nop 1
	v_cndmask_b32_e64 v102, v102, v104, s[0:1]
	v_mul_f32_e32 v103, 0x37800000, v102
	v_cndmask_b32_e32 v102, v102, v103, vcc
	v_cmp_class_f32_e32 vcc, v78, v85
	s_nop 1
	v_cndmask_b32_e32 v78, v102, v78, vcc
	v_div_scale_f32 v102, s[0:1], v78, v78, 1.0
	v_rcp_f32_e32 v103, v102
	v_div_scale_f32 v104, vcc, 1.0, v78, 1.0
	v_fma_f32 v105, -v102, v103, 1.0
	v_fmac_f32_e32 v103, v105, v103
	v_mul_f32_e32 v105, v104, v103
	v_fma_f32 v106, -v102, v105, v104
	v_fmac_f32_e32 v105, v106, v103
	v_fma_f32 v102, -v102, v105, v104
	v_div_fmas_f32 v102, v102, v103, v105
	v_div_fixup_f32 v78, v102, v78, 1.0
	v_pk_mul_f32 v[60:61], v[60:61], v[78:79] op_sel_hi:[1,0]
	v_pk_mul_f32 v[58:59], v[58:59], v[78:79] op_sel_hi:[1,0]
	s_waitcnt vmcnt(13)
	v_pk_mul_f32 v[60:61], v[60:61], v[96:97]
	v_pk_mul_f32 v[58:59], v[58:59], v[94:95]
	s_waitcnt vmcnt(12)
	v_pk_fma_f32 v[60:61], v[60:61], v[92:93], v[100:101]
	v_pk_fma_f32 v[58:59], v[58:59], v[90:91], v[98:99]
	v_pk_mul_f32 v[52:53], v[52:53], v[78:79] op_sel_hi:[1,0]
	v_cvt_pk_bf16_f32 v58, v58, v59
	v_cvt_pk_bf16_f32 v59, v60, v61
	global_store_dwordx2 v[76:77], v[58:59], off
	global_load_dwordx4 v[58:61], v[66:67], off offset:1024
	s_nop 0
	global_load_dwordx4 v[90:93], v87, s[28:29]
	global_load_dwordx4 v[94:97], v86, s[26:27] offset:1024
	v_pk_mul_f32 v[50:51], v[50:51], v[78:79] op_sel_hi:[1,0]
	v_pk_mul_f32 v[36:37], v[36:37], v[78:79] op_sel_hi:[1,0]
	v_pk_mul_f32 v[34:35], v[34:35], v[78:79] op_sel_hi:[1,0]
	v_pk_mul_f32 v[20:21], v[20:21], v[78:79] op_sel_hi:[1,0]
	v_pk_mul_f32 v[18:19], v[18:19], v[78:79] op_sel_hi:[1,0]
	s_waitcnt vmcnt(13)
	v_mul_f32_e32 v98, v47, v47
	v_mul_f32_e32 v99, v49, v49
	s_waitcnt vmcnt(12)
	v_mul_f32_e32 v100, v43, v43
	v_mul_f32_e32 v101, v45, v45
	v_fmac_f32_e32 v98, v46, v46
	v_fmac_f32_e32 v99, v48, v48
	v_fmac_f32_e32 v100, v42, v42
	v_fmac_f32_e32 v101, v44, v44
	s_waitcnt vmcnt(10)
	v_mul_f32_e32 v102, v33, v33
	v_fmac_f32_e32 v102, v32, v32
	s_waitcnt vmcnt(2)
	v_pk_mul_f32 v[50:51], v[50:51], v[58:59]
	v_pk_mul_f32 v[52:53], v[52:53], v[60:61]
	s_waitcnt vmcnt(1)
	v_pk_add_f32 v[58:59], v[92:93], 1.0 op_sel_hi:[1,0]
	v_pk_add_f32 v[60:61], v[90:91], 1.0 op_sel_hi:[1,0]
	s_waitcnt vmcnt(0)
	v_pk_fma_f32 v[52:53], v[52:53], v[58:59], v[96:97]
	v_pk_fma_f32 v[50:51], v[50:51], v[60:61], v[94:95]
	v_mul_f32_e32 v94, v63, v63
	v_cvt_pk_bf16_f32 v50, v50, v51
	v_cvt_pk_bf16_f32 v51, v52, v53
	global_store_dwordx2 v[76:77], v[50:51], off offset:512
	global_load_dwordx4 v[50:53], v[66:67], off offset:2048
	s_nop 0
	global_load_dwordx4 v[58:61], v88, s[28:29]
	global_load_dwordx4 v[90:93], v86, s[26:27] offset:2048
	v_mul_f32_e32 v95, v65, v65
	v_mul_f32_e32 v96, v55, v55
	v_mul_f32_e32 v97, v57, v57
	v_fmac_f32_e32 v94, v62, v62
	v_fmac_f32_e32 v95, v64, v64
	v_fmac_f32_e32 v96, v54, v54
	v_fmac_f32_e32 v97, v56, v56
	v_add_f32_e32 v94, v94, v95
	v_add_f32_e32 v95, v96, v97
	v_add_f32_e32 v96, v98, v99
	v_add_f32_e32 v94, v94, v95
	v_add_f32_e32 v97, v100, v101
	v_add_f32_e32 v94, v94, v96
	v_add_f32_e32 v98, v94, v97
	v_mul_f32_e32 v99, v39, v39
	v_mul_f32_e32 v100, v41, v41
	v_mul_f32_e32 v101, v31, v31
	v_fmac_f32_e32 v99, v38, v38
	v_fmac_f32_e32 v100, v40, v40
	v_fmac_f32_e32 v101, v30, v30
	s_waitcnt vmcnt(2)
	v_pk_mul_f32 v[34:35], v[34:35], v[50:51]
	v_pk_mul_f32 v[36:37], v[36:37], v[52:53]
	s_waitcnt vmcnt(1)
	v_pk_add_f32 v[50:51], v[60:61], 1.0 op_sel_hi:[1,0]
	v_pk_add_f32 v[52:53], v[58:59], 1.0 op_sel_hi:[1,0]
	s_waitcnt vmcnt(0)
	v_pk_fma_f32 v[36:37], v[36:37], v[50:51], v[92:93]
	v_pk_fma_f32 v[34:35], v[34:35], v[52:53], v[90:91]
	v_add_f32_e32 v51, v99, v100
	v_cvt_pk_bf16_f32 v34, v34, v35
	v_cvt_pk_bf16_f32 v35, v36, v37
	global_store_dwordx2 v[76:77], v[34:35], off offset:1024
	global_load_dwordx4 v[58:61], v[66:67], off offset:3072
	global_load_dwordx4 v[90:93], v89, s[28:29]
	global_load_dwordx4 v[94:97], v86, s[26:27] offset:3072
	v_mul_f32_e32 v34, v27, v27
	v_mul_f32_e32 v35, v29, v29
	v_mul_f32_e32 v36, v23, v23
	v_mul_f32_e32 v37, v25, v25
	v_fmac_f32_e32 v34, v26, v26
	v_fmac_f32_e32 v35, v28, v28
	v_fmac_f32_e32 v36, v22, v22
	v_fmac_f32_e32 v37, v24, v24
	v_add_f32_e32 v52, v101, v102
	v_add_f32_e32 v34, v34, v35
	v_add_f32_e32 v35, v36, v37
	v_add_f32_e32 v36, v51, v52
	v_add_f32_e32 v34, v36, v34
	v_add_f32_e32 v34, v34, v35
	v_mul_f32_e32 v35, v15, v15
	v_mul_f32_e32 v36, v17, v17
	v_mul_f32_e32 v37, v11, v11
	v_mul_f32_e32 v51, v13, v13
	v_mul_f32_e32 v52, v7, v7
	v_mul_f32_e32 v53, v9, v9
	v_fmac_f32_e32 v35, v14, v14
	v_fmac_f32_e32 v36, v16, v16
	v_fmac_f32_e32 v37, v10, v10
	v_fmac_f32_e32 v51, v12, v12
	v_mul_f32_e32 v99, v3, v3
	v_mul_f32_e32 v100, v5, v5
	v_fmac_f32_e32 v52, v6, v6
	v_fmac_f32_e32 v53, v8, v8
	v_add_f32_e32 v35, v35, v36
	v_add_f32_e32 v36, v37, v51
	v_fmac_f32_e32 v99, v2, v2
	v_fmac_f32_e32 v100, v4, v4
	v_add_f32_e32 v37, v52, v53
	v_add_f32_e32 v35, v35, v36
	v_add_f32_e32 v51, v99, v100
	v_add_f32_e32 v35, v35, v37
	v_add_f32_e32 v35, v35, v51
	ds_bpermute_b32 v50, v1, v98
	ds_bpermute_b32 v101, v1, v34
	ds_bpermute_b32 v36, v1, v35
	s_waitcnt lgkmcnt(2)
	v_add_f32_e32 v37, v98, v50
	s_waitcnt lgkmcnt(1)
	v_add_f32_e32 v34, v34, v101
	s_waitcnt lgkmcnt(0)
	v_add_f32_e32 v35, v35, v36
	ds_bpermute_b32 v50, v79, v37
	ds_bpermute_b32 v51, v79, v34
	ds_bpermute_b32 v36, v79, v35
	s_waitcnt lgkmcnt(2)
	v_add_f32_e32 v37, v37, v50
	s_waitcnt lgkmcnt(1)
	v_add_f32_e32 v34, v34, v51
	s_waitcnt lgkmcnt(0)
	v_add_f32_e32 v35, v35, v36
	ds_bpermute_b32 v50, v80, v37
	ds_bpermute_b32 v51, v80, v34
	ds_bpermute_b32 v36, v80, v35
	s_waitcnt lgkmcnt(2)
	v_add_f32_e32 v37, v37, v50
	s_waitcnt lgkmcnt(1)
	v_add_f32_e32 v34, v34, v51
	s_waitcnt lgkmcnt(0)
	v_add_f32_e32 v35, v35, v36
	ds_bpermute_b32 v50, v81, v37
	ds_bpermute_b32 v51, v81, v34
	ds_bpermute_b32 v36, v81, v35
	s_waitcnt lgkmcnt(2)
	v_add_f32_e32 v37, v37, v50
	s_waitcnt lgkmcnt(1)
	v_add_f32_e32 v34, v34, v51
	s_waitcnt lgkmcnt(0)
	v_add_f32_e32 v35, v35, v36
	ds_bpermute_b32 v50, v82, v37
	ds_bpermute_b32 v52, v82, v34
	ds_bpermute_b32 v53, v82, v35
	s_waitcnt lgkmcnt(2)
	v_add_f32_e32 v50, v37, v50
	s_waitcnt lgkmcnt(1)
	v_add_f32_e32 v36, v34, v52
	s_waitcnt lgkmcnt(0)
	v_add_f32_e32 v34, v35, v53
	ds_bpermute_b32 v51, v83, v50
	ds_bpermute_b32 v37, v83, v36
	ds_bpermute_b32 v35, v83, v34
	s_waitcnt vmcnt(2)
	v_pk_mul_f32 v[18:19], v[18:19], v[58:59]
	v_pk_mul_f32 v[20:21], v[20:21], v[60:61]
	s_waitcnt vmcnt(1)
	v_pk_add_f32 v[52:53], v[92:93], 1.0 op_sel_hi:[1,0]
	v_pk_add_f32 v[58:59], v[90:91], 1.0 op_sel_hi:[1,0]
	s_waitcnt vmcnt(0)
	v_pk_fma_f32 v[20:21], v[20:21], v[52:53], v[96:97]
	v_pk_fma_f32 v[18:19], v[18:19], v[58:59], v[94:95]
	s_nop 0
	v_cvt_pk_bf16_f32 v18, v18, v19
	v_cvt_pk_bf16_f32 v19, v20, v21
	global_store_dwordx2 v[76:77], v[18:19], off offset:1536
	s_cbranch_scc1 .LBB0_175
	s_ashr_i32 s0, s19, 13
	s_mulk_i32 s0, 0x1800
	s_ashr_i32 s1, s0, 31
	s_lshl_b64 s[0:1], s[0:1], 2
	s_add_u32 s26, s96, s0
	s_addc_u32 s27, s97, s1
	s_add_u32 s28, s26, 0x1000
	global_load_dwordx4 v[18:21], v[66:67], off
	s_addc_u32 s29, s27, 0
	global_load_dwordx4 v[58:61], v86, s[28:29]
	global_load_dwordx4 v[90:93], v86, s[26:27]
	global_load_dwordx4 v[110:113], v[66:67], off offset:1024
	global_load_dwordx4 v[114:117], v87, s[28:29]
	global_load_dwordx4 v[118:121], v86, s[26:27] offset:1024
	global_load_dwordx4 v[122:125], v[66:67], off offset:2048
	global_load_dwordx4 v[126:129], v88, s[28:29]
	global_load_dwordx4 v[130:133], v86, s[26:27] offset:2048
	global_load_dwordx4 v[134:137], v[66:67], off offset:3072
	global_load_dwordx4 v[138:141], v89, s[28:29]
	global_load_dwordx4 v[142:145], v86, s[26:27] offset:3072
	s_waitcnt lgkmcnt(2)
	v_add_f32_e32 v50, v50, v51
	v_fmamk_f32 v50, v50, 0x3a800000, v84
	v_mul_f32_e32 v51, 0x4f800000, v50
	v_cmp_gt_f32_e32 vcc, s7, v50
	s_nop 1
	v_cndmask_b32_e32 v52, v50, v51, vcc
	v_sqrt_f32_e32 v53, v52
	v_lshl_add_u64 v[50:51], s[10:11], 0, v[70:71]
	v_add_u32_e32 v76, -1, v53
	v_add_u32_e32 v77, 1, v53
	v_fma_f32 v78, -v76, v53, v52
	v_fma_f32 v94, -v77, v53, v52
	v_cmp_ge_f32_e64 s[0:1], 0, v78
	s_nop 1
	v_cndmask_b32_e64 v53, v53, v76, s[0:1]
	v_cmp_lt_f32_e64 s[0:1], 0, v94
	s_nop 1
	v_cndmask_b32_e64 v53, v53, v77, s[0:1]
	v_mul_f32_e32 v76, 0x37800000, v53
	v_cndmask_b32_e32 v53, v53, v76, vcc
	v_cmp_class_f32_e32 vcc, v52, v85
	s_nop 1
	v_cndmask_b32_e32 v52, v53, v52, vcc
	v_div_scale_f32 v53, s[0:1], v52, v52, 1.0
	v_rcp_f32_e32 v78, v53
	v_add_co_u32_e32 v76, vcc, s9, v50
	s_nop 1
	v_addc_co_u32_e32 v77, vcc, 0, v51, vcc
	v_fma_f32 v51, -v53, v78, 1.0
	v_div_scale_f32 v50, vcc, 1.0, v52, 1.0
	v_fmac_f32_e32 v78, v51, v78
	v_mul_f32_e32 v51, v50, v78
	v_fma_f32 v94, -v53, v51, v50
	v_fmac_f32_e32 v51, v94, v78
	v_fma_f32 v50, -v53, v51, v50
	v_div_fmas_f32 v50, v50, v78, v51
	v_div_fixup_f32 v78, v50, v52, 1.0
	v_pk_mul_f32 v[50:51], v[64:65], v[78:79] op_sel_hi:[1,0]
	v_pk_mul_f32 v[52:53], v[62:63], v[78:79] op_sel_hi:[1,0]
	v_pk_mul_f32 v[56:57], v[56:57], v[78:79] op_sel_hi:[1,0]
	v_pk_mul_f32 v[54:55], v[54:55], v[78:79] op_sel_hi:[1,0]
	v_pk_mul_f32 v[48:49], v[48:49], v[78:79] op_sel_hi:[1,0]
	v_pk_mul_f32 v[46:47], v[46:47], v[78:79] op_sel_hi:[1,0]
	v_pk_mul_f32 v[44:45], v[44:45], v[78:79] op_sel_hi:[1,0]
	v_pk_mul_f32 v[42:43], v[42:43], v[78:79] op_sel_hi:[1,0]
	s_waitcnt vmcnt(11)
	v_pk_mul_f32 v[18:19], v[52:53], v[18:19]
	v_pk_mul_f32 v[20:21], v[50:51], v[20:21]
	s_waitcnt vmcnt(10)
	v_pk_add_f32 v[50:51], v[60:61], 1.0 op_sel_hi:[1,0]
	v_pk_add_f32 v[52:53], v[58:59], 1.0 op_sel_hi:[1,0]
	s_waitcnt vmcnt(9)
	v_pk_fma_f32 v[20:21], v[20:21], v[50:51], v[92:93]
	v_pk_fma_f32 v[18:19], v[18:19], v[52:53], v[90:91]
	s_nop 0
	v_cvt_pk_bf16_f32 v18, v18, v19
	v_cvt_pk_bf16_f32 v19, v20, v21
	global_store_dwordx2 v[76:77], v[18:19], off
	s_waitcnt vmcnt(9)
	v_pk_mul_f32 v[18:19], v[54:55], v[110:111]
	v_pk_mul_f32 v[20:21], v[56:57], v[112:113]
	s_waitcnt vmcnt(8)
	v_pk_add_f32 v[52:53], v[116:117], 1.0 op_sel_hi:[1,0]
	v_pk_add_f32 v[50:51], v[114:115], 1.0 op_sel_hi:[1,0]
	s_waitcnt vmcnt(7)
	v_pk_fma_f32 v[20:21], v[20:21], v[52:53], v[120:121]
	v_pk_fma_f32 v[18:19], v[18:19], v[50:51], v[118:119]
	s_nop 0
	v_cvt_pk_bf16_f32 v18, v18, v19
	v_cvt_pk_bf16_f32 v19, v20, v21
	global_store_dwordx2 v[76:77], v[18:19], off offset:512
	s_waitcnt vmcnt(7)
	v_pk_mul_f32 v[18:19], v[46:47], v[122:123]
	v_pk_mul_f32 v[20:21], v[48:49], v[124:125]
	s_waitcnt vmcnt(6)
	v_pk_add_f32 v[46:47], v[128:129], 1.0 op_sel_hi:[1,0]
	v_pk_add_f32 v[48:49], v[126:127], 1.0 op_sel_hi:[1,0]
	s_waitcnt vmcnt(5)
	v_pk_fma_f32 v[20:21], v[20:21], v[46:47], v[132:133]
	v_pk_fma_f32 v[18:19], v[18:19], v[48:49], v[130:131]
	s_nop 0
	v_cvt_pk_bf16_f32 v18, v18, v19
	v_cvt_pk_bf16_f32 v19, v20, v21
	global_store_dwordx2 v[76:77], v[18:19], off offset:1024
	s_waitcnt vmcnt(5)
	v_pk_mul_f32 v[18:19], v[42:43], v[134:135]
	v_pk_mul_f32 v[20:21], v[44:45], v[136:137]
	s_waitcnt vmcnt(4)
	v_pk_add_f32 v[42:43], v[140:141], 1.0 op_sel_hi:[1,0]
	v_pk_add_f32 v[44:45], v[138:139], 1.0 op_sel_hi:[1,0]
	s_waitcnt vmcnt(3)
	v_pk_fma_f32 v[20:21], v[20:21], v[42:43], v[144:145]
	v_pk_fma_f32 v[18:19], v[18:19], v[44:45], v[142:143]
	s_nop 0
	v_cvt_pk_bf16_f32 v18, v18, v19
	v_cvt_pk_bf16_f32 v19, v20, v21
	global_store_dwordx2 v[76:77], v[18:19], off offset:1536
	s_andn2_b64 vcc, exec, s[24:25]
	s_cbranch_vccz .LBB0_176

.LBB0_176:
	s_ashr_i32 s0, s22, 13
	s_mulk_i32 s0, 0x1800
	s_ashr_i32 s23, s22, 31
	s_ashr_i32 s1, s0, 31
	s_lshl_b64 s[26:27], s[22:23], 11
	s_lshl_b64 s[0:1], s[0:1], 2
	s_add_u32 s22, s96, s0
	s_addc_u32 s23, s97, s1
	s_add_u32 s24, s22, 0x1000
	global_load_dwordx4 v[18:21], v[66:67], off
	s_addc_u32 s25, s23, 0
	global_load_dwordx4 v[42:45], v86, s[24:25]
	global_load_dwordx4 v[46:49], v86, s[22:23]
	global_load_dwordx4 v[110:113], v[66:67], off offset:1024
	global_load_dwordx4 v[114:117], v87, s[24:25]
	global_load_dwordx4 v[118:121], v86, s[22:23] offset:1024
	global_load_dwordx4 v[122:125], v[66:67], off offset:2048
	global_load_dwordx4 v[126:129], v88, s[24:25]
	global_load_dwordx4 v[130:133], v86, s[22:23] offset:2048
	global_load_dwordx4 v[134:137], v[66:67], off offset:3072
	global_load_dwordx4 v[138:141], v89, s[24:25]
	global_load_dwordx4 v[142:145], v86, s[22:23] offset:3072
	s_waitcnt lgkmcnt(1)
	v_add_f32_e32 v36, v36, v37
	v_fmamk_f32 v36, v36, 0x3a800000, v84
	v_mul_f32_e32 v37, 0x4f800000, v36
	v_cmp_gt_f32_e32 vcc, s7, v36
	s_nop 1
	v_cndmask_b32_e32 v36, v36, v37, vcc
	v_sqrt_f32_e32 v37, v36
	s_nop 0
	v_add_u32_e32 v50, -1, v37
	v_add_u32_e32 v51, 1, v37
	v_fma_f32 v52, -v50, v37, v36
	v_fma_f32 v53, -v51, v37, v36
	v_cmp_ge_f32_e64 s[0:1], 0, v52
	s_nop 1
	v_cndmask_b32_e64 v37, v37, v50, s[0:1]
	v_cmp_lt_f32_e64 s[0:1], 0, v53
	s_nop 1
	v_cndmask_b32_e64 v37, v37, v51, s[0:1]
	v_mul_f32_e32 v50, 0x37800000, v37
	v_cndmask_b32_e32 v37, v37, v50, vcc
	v_cmp_class_f32_e32 vcc, v36, v85
	v_lshl_add_u64 v[50:51], v[72:73], 0, s[26:27]
	s_nop 0
	v_cndmask_b32_e32 v36, v37, v36, vcc
	v_div_scale_f32 v37, s[0:1], v36, v36, 1.0
	v_rcp_f32_e32 v52, v37
	v_div_scale_f32 v53, vcc, 1.0, v36, 1.0
	v_fma_f32 v54, -v37, v52, 1.0
	v_fmac_f32_e32 v52, v54, v52
	v_mul_f32_e32 v54, v53, v52
	v_fma_f32 v55, -v37, v54, v53
	v_fmac_f32_e32 v54, v55, v52
	v_fma_f32 v37, -v37, v54, v53
	v_div_fmas_f32 v37, v37, v52, v54
	v_div_fixup_f32 v52, v37, v36, 1.0
	v_pk_mul_f32 v[36:37], v[40:41], v[52:53] op_sel_hi:[1,0]
	v_pk_mul_f32 v[38:39], v[38:39], v[52:53] op_sel_hi:[1,0]
	v_pk_mul_f32 v[32:33], v[32:33], v[52:53] op_sel_hi:[1,0]
	v_pk_mul_f32 v[30:31], v[30:31], v[52:53] op_sel_hi:[1,0]
	v_pk_mul_f32 v[28:29], v[28:29], v[52:53] op_sel_hi:[1,0]
	v_pk_mul_f32 v[26:27], v[26:27], v[52:53] op_sel_hi:[1,0]
	v_pk_mul_f32 v[24:25], v[24:25], v[52:53] op_sel_hi:[1,0]
	v_pk_mul_f32 v[22:23], v[22:23], v[52:53] op_sel_hi:[1,0]
	s_waitcnt vmcnt(11)
	v_pk_mul_f32 v[18:19], v[38:39], v[18:19]
	v_pk_mul_f32 v[20:21], v[36:37], v[20:21]
	s_waitcnt vmcnt(10)
	v_pk_add_f32 v[36:37], v[44:45], 1.0 op_sel_hi:[1,0]
	v_pk_add_f32 v[38:39], v[42:43], 1.0 op_sel_hi:[1,0]
	s_waitcnt vmcnt(9)
	v_pk_fma_f32 v[20:21], v[20:21], v[36:37], v[48:49]
	v_pk_fma_f32 v[18:19], v[18:19], v[38:39], v[46:47]
	s_nop 0
	v_cvt_pk_bf16_f32 v18, v18, v19
	v_cvt_pk_bf16_f32 v19, v20, v21
	global_store_dwordx2 v[50:51], v[18:19], off
	s_waitcnt vmcnt(9)
	v_pk_mul_f32 v[18:19], v[30:31], v[110:111]
	v_pk_mul_f32 v[20:21], v[32:33], v[112:113]
	s_waitcnt vmcnt(8)
	v_pk_add_f32 v[30:31], v[116:117], 1.0 op_sel_hi:[1,0]
	v_pk_add_f32 v[32:33], v[114:115], 1.0 op_sel_hi:[1,0]
	s_waitcnt vmcnt(7)
	v_pk_fma_f32 v[20:21], v[20:21], v[30:31], v[120:121]
	v_pk_fma_f32 v[18:19], v[18:19], v[32:33], v[118:119]
	s_nop 0
	v_cvt_pk_bf16_f32 v18, v18, v19
	v_cvt_pk_bf16_f32 v19, v20, v21
	global_store_dwordx2 v[50:51], v[18:19], off offset:512
	s_waitcnt vmcnt(7)
	v_pk_mul_f32 v[18:19], v[26:27], v[122:123]
	v_pk_mul_f32 v[20:21], v[28:29], v[124:125]
	s_waitcnt vmcnt(6)
	v_pk_add_f32 v[26:27], v[128:129], 1.0 op_sel_hi:[1,0]
	v_pk_add_f32 v[28:29], v[126:127], 1.0 op_sel_hi:[1,0]
	s_waitcnt vmcnt(5)
	v_pk_fma_f32 v[20:21], v[20:21], v[26:27], v[132:133]
	v_pk_fma_f32 v[18:19], v[18:19], v[28:29], v[130:131]
	s_nop 0
	v_cvt_pk_bf16_f32 v18, v18, v19
	v_cvt_pk_bf16_f32 v19, v20, v21
	global_store_dwordx2 v[50:51], v[18:19], off offset:1024
	s_waitcnt vmcnt(5)
	v_pk_mul_f32 v[18:19], v[22:23], v[134:135]
	v_pk_mul_f32 v[20:21], v[24:25], v[136:137]
	s_waitcnt vmcnt(4)
	v_pk_add_f32 v[22:23], v[140:141], 1.0 op_sel_hi:[1,0]
	v_pk_add_f32 v[24:25], v[138:139], 1.0 op_sel_hi:[1,0]
	s_waitcnt vmcnt(3)
	v_pk_fma_f32 v[20:21], v[20:21], v[22:23], v[144:145]
	v_pk_fma_f32 v[18:19], v[18:19], v[24:25], v[142:143]
	s_nop 0
	v_cvt_pk_bf16_f32 v18, v18, v19
	v_cvt_pk_bf16_f32 v19, v20, v21
	global_store_dwordx2 v[50:51], v[18:19], off offset:1536
	s_andn2_b64 vcc, exec, s[20:21]
	s_cbranch_vccnz .LBB0_171
.LBB0_177:
	s_ashr_i32 s0, s18, 13
	s_mulk_i32 s0, 0x1800
	s_ashr_i32 s19, s18, 31
	s_ashr_i32 s1, s0, 31
	s_lshl_b64 s[22:23], s[18:19], 11
	s_lshl_b64 s[0:1], s[0:1], 2
	s_add_u32 s18, s96, s0
	s_addc_u32 s19, s97, s1
	s_add_u32 s20, s18, 0x1000
	global_load_dwordx4 v[18:21], v[66:67], off
	s_addc_u32 s21, s19, 0
	global_load_dwordx4 v[22:25], v86, s[20:21]
	global_load_dwordx4 v[26:29], v86, s[18:19]
	global_load_dwordx4 v[110:113], v[66:67], off offset:1024
	global_load_dwordx4 v[114:117], v87, s[20:21]
	global_load_dwordx4 v[118:121], v86, s[18:19] offset:1024
	global_load_dwordx4 v[122:125], v[66:67], off offset:2048
	global_load_dwordx4 v[126:129], v88, s[20:21]
	global_load_dwordx4 v[130:133], v86, s[18:19] offset:2048
	global_load_dwordx4 v[134:137], v[66:67], off offset:3072
	global_load_dwordx4 v[138:141], v89, s[20:21]
	global_load_dwordx4 v[142:145], v86, s[18:19] offset:3072
	s_waitcnt lgkmcnt(0)
	v_add_f32_e32 v30, v34, v35
	v_fmamk_f32 v30, v30, 0x3a800000, v84
	v_mul_f32_e32 v31, 0x4f800000, v30
	v_cmp_gt_f32_e32 vcc, s7, v30
	s_nop 1
	v_cndmask_b32_e32 v30, v30, v31, vcc
	v_sqrt_f32_e32 v31, v30
	s_nop 0
	v_add_u32_e32 v32, -1, v31
	v_add_u32_e32 v33, 1, v31
	v_fma_f32 v34, -v32, v31, v30
	v_fma_f32 v35, -v33, v31, v30
	v_cmp_ge_f32_e64 s[0:1], 0, v34
	s_nop 1
	v_cndmask_b32_e64 v31, v31, v32, s[0:1]
	v_cmp_lt_f32_e64 s[0:1], 0, v35
	s_nop 1
	v_cndmask_b32_e64 v31, v31, v33, s[0:1]
	v_mul_f32_e32 v32, 0x37800000, v31
	v_cndmask_b32_e32 v31, v31, v32, vcc
	v_cmp_class_f32_e32 vcc, v30, v85
	s_nop 1
	v_cndmask_b32_e32 v32, v31, v30, vcc
	v_div_scale_f32 v33, s[0:1], v32, v32, 1.0
	v_rcp_f32_e32 v34, v33
	v_div_scale_f32 v35, vcc, 1.0, v32, 1.0
	v_lshl_add_u64 v[30:31], v[72:73], 0, s[22:23]
	v_fma_f32 v36, -v33, v34, 1.0
	v_fmac_f32_e32 v34, v36, v34
	v_mul_f32_e32 v36, v35, v34
	v_fma_f32 v37, -v33, v36, v35
	v_fmac_f32_e32 v36, v37, v34
	v_fma_f32 v33, -v33, v36, v35
	v_div_fmas_f32 v33, v33, v34, v36
	v_div_fixup_f32 v32, v33, v32, 1.0
	v_pk_mul_f32 v[16:17], v[16:17], v[32:33] op_sel_hi:[1,0]
	v_pk_mul_f32 v[14:15], v[14:15], v[32:33] op_sel_hi:[1,0]
	v_pk_mul_f32 v[12:13], v[12:13], v[32:33] op_sel_hi:[1,0]
	v_pk_mul_f32 v[10:11], v[10:11], v[32:33] op_sel_hi:[1,0]
	v_pk_mul_f32 v[8:9], v[8:9], v[32:33] op_sel_hi:[1,0]
	v_pk_mul_f32 v[6:7], v[6:7], v[32:33] op_sel_hi:[1,0]
	v_pk_mul_f32 v[4:5], v[4:5], v[32:33] op_sel_hi:[1,0]
	v_pk_mul_f32 v[2:3], v[2:3], v[32:33] op_sel_hi:[1,0]
	s_waitcnt vmcnt(11)
	v_pk_mul_f32 v[14:15], v[14:15], v[18:19]
	v_pk_mul_f32 v[16:17], v[16:17], v[20:21]
	s_waitcnt vmcnt(10)
	v_pk_add_f32 v[18:19], v[24:25], 1.0 op_sel_hi:[1,0]
	v_pk_add_f32 v[20:21], v[22:23], 1.0 op_sel_hi:[1,0]
	s_waitcnt vmcnt(9)
	v_pk_fma_f32 v[16:17], v[16:17], v[18:19], v[28:29]
	v_pk_fma_f32 v[14:15], v[14:15], v[20:21], v[26:27]
	s_nop 0
	v_cvt_pk_bf16_f32 v14, v14, v15
	v_cvt_pk_bf16_f32 v15, v16, v17
	global_store_dwordx2 v[30:31], v[14:15], off
	s_waitcnt vmcnt(9)
	v_pk_mul_f32 v[10:11], v[10:11], v[110:111]
	v_pk_mul_f32 v[12:13], v[12:13], v[112:113]
	s_waitcnt vmcnt(8)
	v_pk_add_f32 v[14:15], v[116:117], 1.0 op_sel_hi:[1,0]
	v_pk_add_f32 v[16:17], v[114:115], 1.0 op_sel_hi:[1,0]
	s_waitcnt vmcnt(7)
	v_pk_fma_f32 v[12:13], v[12:13], v[14:15], v[120:121]
	v_pk_fma_f32 v[10:11], v[10:11], v[16:17], v[118:119]
	s_nop 0
	v_cvt_pk_bf16_f32 v10, v10, v11
	v_cvt_pk_bf16_f32 v11, v12, v13
	global_store_dwordx2 v[30:31], v[10:11], off offset:512
	s_waitcnt vmcnt(7)
	v_pk_mul_f32 v[6:7], v[6:7], v[122:123]
	v_pk_mul_f32 v[8:9], v[8:9], v[124:125]
	s_waitcnt vmcnt(6)
	v_pk_add_f32 v[10:11], v[128:129], 1.0 op_sel_hi:[1,0]
	v_pk_add_f32 v[12:13], v[126:127], 1.0 op_sel_hi:[1,0]
	s_waitcnt vmcnt(5)
	v_pk_fma_f32 v[8:9], v[8:9], v[10:11], v[132:133]
	v_pk_fma_f32 v[6:7], v[6:7], v[12:13], v[130:131]
	s_nop 0
	v_cvt_pk_bf16_f32 v6, v6, v7
	v_cvt_pk_bf16_f32 v7, v8, v9
	global_store_dwordx2 v[30:31], v[6:7], off offset:1024
	s_waitcnt vmcnt(5)
	v_pk_mul_f32 v[2:3], v[2:3], v[134:135]
	v_pk_mul_f32 v[4:5], v[4:5], v[136:137]
	s_waitcnt vmcnt(4)
	v_pk_add_f32 v[6:7], v[140:141], 1.0 op_sel_hi:[1,0]
	v_pk_add_f32 v[8:9], v[138:139], 1.0 op_sel_hi:[1,0]
	s_waitcnt vmcnt(3)
	v_pk_fma_f32 v[4:5], v[4:5], v[6:7], v[144:145]
	v_pk_fma_f32 v[2:3], v[2:3], v[8:9], v[142:143]
	s_nop 0
	v_cvt_pk_bf16_f32 v2, v2, v3
	v_cvt_pk_bf16_f32 v3, v4, v5
	global_store_dwordx2 v[30:31], v[2:3], off offset:1536
	s_branch .LBB0_171
